# LN+router pass 2: hand-written software-pipelined logits loop (step s+1 loads in flight during step s MFMAs; two register sets) replaces the compiler's load-wait-MFMA loop
# speedup vs baseline: 1.0036x; 1.0036x over previous
.LBB0_935:
	v_add_co_u32_e32 v40, vcc, 0x5f61ba00, v36
	s_mov_b64 s[6:7], 0x1000
	s_mov_b32 s4, 0
	v_addc_co_u32_e32 v41, vcc, 0, v37, vcc
	v_add_u32_e32 v46, -14, v46
	v_xor_b32_e32 v2, v46, v45
	v_lshl_add_u32 v2, v2, 4, v44
	global_load_dwordx4 v[48:51], v[38:39], off offset:-128
	ds_read_b128 v[52:55], v2
	global_load_dwordx4 v[56:59], v[40:41], off
	global_load_dwordx4 v[60:63], v[40:41], off offset:1024
	global_load_dwordx4 v[64:67], v[40:41], off offset:2048
	global_load_dwordx4 v[68:71], v[40:41], off offset:3072
	v_add_u32_e32 v46, 2, v46
	v_lshl_add_u64 v[38:39], v[38:39], 0, 32
	v_lshl_add_u64 v[40:41], v[40:41], 0, s[6:7]
.Lrt_loop:
	v_xor_b32_e32 v2, v46, v45
	v_lshl_add_u32 v2, v2, 4, v44
	global_load_dwordx4 v[160:163], v[38:39], off offset:-128
	ds_read_b128 v[164:167], v2
	global_load_dwordx4 v[168:171], v[40:41], off
	global_load_dwordx4 v[172:175], v[40:41], off offset:1024
	global_load_dwordx4 v[176:179], v[40:41], off offset:2048
	global_load_dwordx4 v[180:183], v[40:41], off offset:3072
	v_add_u32_e32 v46, 2, v46
	v_lshl_add_u64 v[38:39], v[38:39], 0, 32
	v_lshl_add_u64 v[40:41], v[40:41], 0, s[6:7]
	s_waitcnt vmcnt(5) lgkmcnt(1)
	v_mfma_f32_32x32x16_bf16 v[4:19], v[48:51], v[56:59], v[4:19]
	v_mfma_f32_32x32x16_bf16 v[20:35], v[48:51], v[64:67], v[20:35]
	v_mfma_f32_32x32x16_bf16 v[4:19], v[48:51], v[60:63], v[4:19]
	v_mfma_f32_32x32x16_bf16 v[20:35], v[48:51], v[68:71], v[20:35]
	v_mfma_f32_32x32x16_bf16 v[4:19], v[52:55], v[56:59], v[4:19]
	v_mfma_f32_32x32x16_bf16 v[20:35], v[52:55], v[64:67], v[20:35]
	v_xor_b32_e32 v2, v46, v45
	v_lshl_add_u32 v2, v2, 4, v44
	global_load_dwordx4 v[48:51], v[38:39], off offset:-128
	ds_read_b128 v[52:55], v2
	global_load_dwordx4 v[56:59], v[40:41], off
	global_load_dwordx4 v[60:63], v[40:41], off offset:1024
	global_load_dwordx4 v[64:67], v[40:41], off offset:2048
	global_load_dwordx4 v[68:71], v[40:41], off offset:3072
	v_add_u32_e32 v46, 2, v46
	v_lshl_add_u64 v[38:39], v[38:39], 0, 32
	v_lshl_add_u64 v[40:41], v[40:41], 0, s[6:7]
	s_waitcnt vmcnt(5) lgkmcnt(1)
	v_mfma_f32_32x32x16_bf16 v[4:19], v[160:163], v[168:171], v[4:19]
	v_mfma_f32_32x32x16_bf16 v[20:35], v[160:163], v[176:179], v[20:35]
	v_mfma_f32_32x32x16_bf16 v[4:19], v[160:163], v[172:175], v[4:19]
	v_mfma_f32_32x32x16_bf16 v[20:35], v[160:163], v[180:183], v[20:35]
	v_mfma_f32_32x32x16_bf16 v[4:19], v[164:167], v[168:171], v[4:19]
	v_mfma_f32_32x32x16_bf16 v[20:35], v[164:167], v[176:179], v[20:35]
	s_add_u32 s4, s4, 1
	s_cmp_lt_u32 s4, 8
	s_cbranch_scc1 .Lrt_loop
	s_waitcnt vmcnt(0) lgkmcnt(0)
	s_lshl_b32 s34, s90, 2
	v_readlane_b32 s68, v251, 31
	s_lshl_b64 s[4:5], s[34:35], 2
	v_readlane_b32 s74, v251, 37
	v_readlane_b32 s75, v251, 38
	s_add_u32 s4, s74, s4
	s_addc_u32 s5, s75, s5
	s_lshl_b32 s34, s90, 5
	v_readlane_b32 s78, v251, 41
	s_lshl_b64 s[6:7], s[34:35], 2
	v_readlane_b32 s79, v251, 42
	s_add_u32 s6, s78, s6
	s_addc_u32 s7, s79, s7
	s_and_b32 s8, s14, 0x1ffffc0
	v_or_b32_e32 v2, s8, v42
	v_lshlrev_b32_e32 v2, 7, v2
	v_lshlrev_b32_e32 v36, 4, v43
	s_waitcnt lgkmcnt(0)
	s_barrier
	v_add3_u32 v2, 0, v2, v36
	ds_write_b128 v2, v[4:7]
	ds_write_b128 v2, v[20:23] offset:4096
	ds_write_b128 v2, v[8:11] offset:32
	ds_write_b128 v2, v[24:27] offset:4128
	ds_write_b128 v2, v[12:15] offset:64
	ds_write_b128 v2, v[28:31] offset:4160
	ds_write_b128 v2, v[16:19] offset:96
	ds_write_b128 v2, v[32:35] offset:4192
	v_ashrrev_i32_e32 v4, 5, v1
	v_cmp_lt_i32_e32 vcc, 3, v4
	v_readlane_b32 s69, v251, 32
	v_readlane_b32 s70, v251, 33
	v_readlane_b32 s71, v251, 34
	v_readlane_b32 s72, v251, 35
	v_readlane_b32 s73, v251, 36
	v_readlane_b32 s76, v251, 39
	v_readlane_b32 s77, v251, 40
	v_readlane_b32 s80, v251, 43
	v_readlane_b32 s81, v251, 44
	v_readlane_b32 s82, v251, 45
	v_readlane_b32 s83, v251, 46
	s_waitcnt lgkmcnt(0)
	s_barrier
	s_and_saveexec_b64 s[8:9], vcc
	s_xor_b64 s[8:9], exec, s[8:9]
	s_cbranch_execz .LBB0_940
	v_cmp_gt_u32_e32 vcc, 36, v4
	v_mov_b32_e32 v2, 0
	s_and_saveexec_b64 s[10:11], vcc
	s_cbranch_execz .LBB0_939
	v_mov_b32_e32 v5, v3
	v_lshl_add_u64 v[6:7], v[4:5], 2, s[6:7]
	global_load_dword v2, v[6:7], off offset:-16
